# v43 + in_proj accumulator zeroing with 63 v_mov_b64 instead of 127 v_mov_b32
# speedup vs baseline: 1.0181x; 1.0181x over previous
;     __device__ __forceinline__ const char* a_base(const Unit& u) const { if constexpr (G1) return A; else return A + (size_t)u.row0 * 256; }
;     ...
;     for (;;) {
;         const bool has_next = S.next(ui + 1, nxt);
;         const char* nA = has_next ? S.a_base(nxt) : cA; const char* nB = has_next ? S.b_base(nxt) : cB;
;         const bool full = cur.nv > 128;
;         if constexpr (GATHER) { if (has_next) S.a_voff(nxt, vn); else { vn[0][0] = va[0][0]; vn[0][1] = va[0][1]; vn[1][0] = va[1][0]; vn[1][1] = va[1][1]; } }
; #pragma unroll 1
;         for (int t = 0; t < nt; t += 2) {
;             const bool last = (t == nt - 2);
;             const char* a1 = cA + (size_t)(t + 1) * kstep;
;             const char* a2 = last ? nA : cA + (size_t)(t + 2) * kstep; const char* b2 = last ? nB : cB + (size_t)(t + 2) * kstep;
;     ...
; #pragma unroll
;         for (int a = 0; a < 2; ++a)
; #pragma unroll
;             for (int b = 0; b < 2; ++b)
; #pragma unroll
;                 for (int m = 0; m < 4; ++m)
; #pragma unroll
;                     for (int n = 0; n < 2; ++n) acc[a][b][m][n] = (f32x4){0.f, 0.f, 0.f, 0.f};
;         cur = nxt; cA = nA; cB = nB; ++ui;
.LBB0_195:
	s_ashr_i32 s23, s22, 31
	s_lshl_b64 s[24:25], s[22:23], 18
	s_add_u32 s24, s37, s24
	s_addc_u32 s25, s38, s25
	s_and_b64 s[26:27], s[4:5], exec
	s_cselect_b32 s23, s25, s29
	s_cselect_b32 s55, s24, s28
	s_ashr_i32 s19, s18, 31
	s_lshl_b64 s[26:27], s[18:19], 18
	s_add_u32 s26, s39, s26
	s_addc_u32 s27, s41, s27
	s_and_b64 s[34:35], s[4:5], exec
	s_cselect_b32 s19, s27, s31
	s_cselect_b32 s56, s26, s30
	s_add_u32 s28, s28, 0x20080
	s_addc_u32 s29, s29, 0
	s_add_u32 s58, s30, 0x100
	v_mov_b32_e32 v34, 0
	s_addc_u32 s59, s31, 0
	s_mov_b32 s64, -2
	v_mov_b32_e32 v35, v34
	v_mov_b64_e32 v[36:37], v[34:35]
	v_mov_b64_e32 v[38:39], v[34:35]
	v_mov_b64_e32 v[40:41], v[34:35]
	v_mov_b64_e32 v[42:43], v[34:35]
	v_mov_b64_e32 v[44:45], v[34:35]
	v_mov_b64_e32 v[46:47], v[34:35]
	v_mov_b64_e32 v[48:49], v[34:35]
	v_mov_b64_e32 v[50:51], v[34:35]
	v_mov_b64_e32 v[52:53], v[34:35]
	v_mov_b64_e32 v[54:55], v[34:35]
	v_mov_b64_e32 v[56:57], v[34:35]
	v_mov_b64_e32 v[58:59], v[34:35]
	v_mov_b64_e32 v[60:61], v[34:35]
	v_mov_b64_e32 v[62:63], v[34:35]
	v_mov_b64_e32 v[64:65], v[34:35]
	v_mov_b64_e32 v[66:67], v[34:35]
	v_mov_b64_e32 v[68:69], v[34:35]
	v_mov_b64_e32 v[70:71], v[34:35]
	v_mov_b64_e32 v[72:73], v[34:35]
	v_mov_b64_e32 v[74:75], v[34:35]
	v_mov_b64_e32 v[76:77], v[34:35]
	v_mov_b64_e32 v[78:79], v[34:35]
	v_mov_b64_e32 v[80:81], v[34:35]
	v_mov_b64_e32 v[82:83], v[34:35]
	v_mov_b64_e32 v[84:85], v[34:35]
	v_mov_b64_e32 v[86:87], v[34:35]
	v_mov_b64_e32 v[88:89], v[34:35]
	v_mov_b64_e32 v[90:91], v[34:35]
	v_mov_b64_e32 v[92:93], v[34:35]
	v_mov_b64_e32 v[94:95], v[34:35]
	v_mov_b64_e32 v[96:97], v[34:35]
	v_mov_b64_e32 v[98:99], v[34:35]
	v_mov_b64_e32 v[100:101], v[34:35]
	v_mov_b64_e32 v[102:103], v[34:35]
	v_mov_b64_e32 v[104:105], v[34:35]
	v_mov_b64_e32 v[106:107], v[34:35]
	v_mov_b64_e32 v[108:109], v[34:35]
	v_mov_b64_e32 v[110:111], v[34:35]
	v_mov_b64_e32 v[112:113], v[34:35]
	v_mov_b64_e32 v[114:115], v[34:35]
	v_mov_b64_e32 v[116:117], v[34:35]
	v_mov_b64_e32 v[118:119], v[34:35]
	v_mov_b64_e32 v[120:121], v[34:35]
	v_mov_b64_e32 v[122:123], v[34:35]
	v_mov_b64_e32 v[124:125], v[34:35]
	v_mov_b64_e32 v[126:127], v[34:35]
	v_mov_b64_e32 v[128:129], v[34:35]
	v_mov_b64_e32 v[130:131], v[34:35]
	v_mov_b64_e32 v[132:133], v[34:35]
	v_mov_b64_e32 v[134:135], v[34:35]
	v_mov_b64_e32 v[136:137], v[34:35]
	v_mov_b64_e32 v[138:139], v[34:35]
	v_mov_b64_e32 v[140:141], v[34:35]
	v_mov_b64_e32 v[142:143], v[34:35]
	v_mov_b64_e32 v[144:145], v[34:35]
	v_mov_b64_e32 v[146:147], v[34:35]
	v_mov_b64_e32 v[148:149], v[34:35]
	v_mov_b64_e32 v[150:151], v[34:35]
	v_mov_b64_e32 v[152:153], v[34:35]
	v_mov_b64_e32 v[154:155], v[34:35]
	v_mov_b64_e32 v[156:157], v[34:35]
	v_mov_b64_e32 v[158:159], v[34:35]
	v_mov_b64_e32 v[160:161], v[34:35]
